# new agg2: double-buffered row gathers (two stage buffers, counted waits), el broadcast via DPP row_newbcast, bias parked in LDS
# speedup vs baseline: 1.0407x; 1.0122x over previous
_Z5k_aggILi1ELi40ELi5ELi5ELb1EEvPKiPKtPKDF16_PKfS7_S7_PvS5_S7_S7_PDF16_PfSA_:
	v_lshrrev_b32_e32 v46, 6, v0
	s_lshl_b32 s3, s2, 2
	v_readfirstlane_b32 s25, v46
	s_load_dwordx4 s[4:7], s[0:1], 0x0
	s_load_dwordx2 s[8:9], s[0:1], 0x10
	s_load_dwordx2 s[12:13], s[0:1], 0x20
	s_load_dwordx4 s[16:19], s[0:1], 0x28
	s_load_dword s20, s[0:1], 0x68
	s_add_i32 s25, s25, s3
	s_cmpk_ge_i32 s25, 0x30d4
	s_cbranch_scc1 .Lagg2n_end
	v_and_b32_e32 v52, 15, v0
	v_bfe_u32 v53, v0, 4, 2
	v_lshrrev_b32_e32 v54, 3, v52
	v_and_b32_e32 v55, 7, v52
	v_min_u32_e32 v47, 5, v55
	v_lshlrev_b32_e32 v56, 4, v47
	v_lshl_or_b32 v47, v46, 2, v53
	v_mul_u32_u24_e32 v47, 0x110, v47
	v_lshl_add_u32 v57, v52, 2, v47
	v_lshl_add_u32 v58, v54, 4, v47
	v_cmp_gt_u32_e32 vcc, 5, v52
	v_min_u32_e32 v47, 4, v55
	v_lshlrev_b32_e32 v47, 5, v47
	s_mov_b64 s[26:27], vcc
	v_mov_b32_e32 v51, 0xff800000
	v_mul_u32_u24_e32 v50, 0xa0, v46
	v_add_u32_e32 v50, v50, v47
	v_add_u32_e32 v50, 0x1100, v50
	v_and_b32_e32 v49, 63, v0
	v_cmp_gt_u32_e64 s[34:35], 5, v49
	s_waitcnt lgkmcnt(0)
	s_add_u32 s12, s12, 0x1da1c0
	s_addc_u32 s13, s13, 0
	s_lshl_b32 s11, s20, 2
	global_load_dwordx4 v[8:11], v47, s[16:17]
	global_load_dwordx4 v[12:15], v47, s[16:17] offset:16
	v_lshl_or_b32 v59, s25, 2, v53
	v_lshlrev_b32_e32 v47, 2, v59
	global_load_dwordx2 v[60:61], v47, s[4:5]
	s_add_i32 s28, s25, s11
	s_min_i32 s28, s28, 0x30d3
	v_lshl_or_b32 v48, s28, 2, v53
	v_lshlrev_b32_e32 v47, 2, v48
	global_load_dwordx2 v[62:63], v47, s[4:5]
	v_lshlrev_b32_e32 v47, 1, v59
	global_load_ushort v70, v47, s[12:13]
	s_waitcnt vmcnt(2)
	v_add_u32_e32 v46, -1, v61
	v_add_u32_e32 v47, v60, v52
	v_min_i32_e32 v48, v47, v46
	v_max_i32_e32 v48, 0, v48
	v_lshlrev_b32_e32 v48, 1, v48
	global_load_ushort v66, v48, s[6:7]
	v_add_u32_e32 v48, 16, v47
	v_min_i32_e32 v48, v48, v46
	v_max_i32_e32 v48, 0, v48
	v_lshlrev_b32_e32 v48, 1, v48
	global_load_ushort v67, v48, s[6:7]
	v_add_u32_e32 v48, 32, v47
	v_min_i32_e32 v48, v48, v46
	v_max_i32_e32 v48, 0, v48
	v_lshlrev_b32_e32 v48, 1, v48
	global_load_ushort v68, v48, s[6:7]
	v_add_u32_e32 v48, 48, v47
	v_min_i32_e32 v48, v48, v46
	v_max_i32_e32 v48, 0, v48
	v_lshlrev_b32_e32 v48, 1, v48
	global_load_ushort v69, v48, s[6:7]
	s_waitcnt vmcnt(0)
	s_and_saveexec_b64 s[28:29], s[34:35]
	ds_write_b128 v50, v[8:11]
	ds_write_b128 v50, v[12:15] offset:16
	s_mov_b64 exec, s[28:29]

.Lagg2n_pass:
	v_mov_b32_e32 v75, v58
	ds_read_b128 v[42:45], v75
	s_waitcnt lgkmcnt(0)
	v_add_u32_e32 v42, v42, v56
	v_add_u32_e32 v43, v43, v56
	v_add_u32_e32 v44, v44, v56
	v_add_u32_e32 v45, v45, v56
	global_load_dwordx4 v[0:3], v42, s[8:9]
	global_load_dwordx4 v[4:7], v43, s[8:9]
	global_load_dwordx4 v[8:11], v44, s[8:9]
	global_load_dwordx4 v[12:15], v45, s[8:9]
	v_add_u32_e32 v75, 32, v75
	ds_read_b128 v[42:45], v75
	s_waitcnt lgkmcnt(0)
	v_add_u32_e32 v42, v42, v56
	v_add_u32_e32 v43, v43, v56
	v_add_u32_e32 v44, v44, v56
	v_add_u32_e32 v45, v45, v56
	global_load_dwordx4 v[34:37], v42, s[8:9]
	global_load_dwordx4 v[38:41], v43, s[8:9]
	global_load_dwordx4 v[20:23], v44, s[8:9]
	global_load_dwordx4 v[76:79], v45, s[8:9]
	v_add_u32_e32 v75, 32, v75
	v_subrev_u32_e32 v73, s22, v72
	v_med3_i32 v73, v73, 0, 64
	v_lshlrev_b32_e32 v46, 2, v54
	v_sub_u32_e32 v74, v73, v46
	s_sub_i32 s28, s21, s22
	s_min_i32 s28, s28, 64
	s_add_i32 s28, s28, 7
	s_lshr_b32 s23, s28, 3
	s_max_i32 s23, s23, 2
	s_mov_b32 s24, 0
.Lagg2n_loop:
	s_add_i32 s28, s24, 1
	s_cmp_lt_i32 s28, s23
	s_cbranch_scc1 .Lagg2n_w4_a
	s_waitcnt vmcnt(0)
.Lagg2n_w4_a:
	s_waitcnt vmcnt(4)
	v_mov_b32_dpp v16, v0 row_newbcast:5 row_mask:0xf bank_mask:0x3
	v_mov_b32_dpp v16, v0 row_newbcast:13 row_mask:0xf bank_mask:0xc
	v_mov_b32_dpp v17, v4 row_newbcast:5 row_mask:0xf bank_mask:0x3
	v_mov_b32_dpp v17, v4 row_newbcast:13 row_mask:0xf bank_mask:0xc
	v_mov_b32_dpp v18, v8 row_newbcast:5 row_mask:0xf bank_mask:0x3
	v_mov_b32_dpp v18, v8 row_newbcast:13 row_mask:0xf bank_mask:0xc
	v_mov_b32_dpp v19, v12 row_newbcast:5 row_mask:0xf bank_mask:0x3
	v_mov_b32_dpp v19, v12 row_newbcast:13 row_mask:0xf bank_mask:0xc
	s_nop 0
	v_fma_mix_f32 v16, v16, 1.0, v71 op_sel_hi:[1,0,0]
	v_fma_mix_f32 v17, v17, 1.0, v71 op_sel_hi:[1,0,0]
	v_fma_mix_f32 v18, v18, 1.0, v71 op_sel_hi:[1,0,0]
	v_fma_mix_f32 v19, v19, 1.0, v71 op_sel_hi:[1,0,0]
	v_mul_f32_e32 v46, 0x3e4ccccd, v16
	v_mul_f32_e32 v47, 0x3e4ccccd, v17
	v_mul_f32_e32 v48, 0x3e4ccccd, v18
	v_mul_f32_e32 v49, 0x3e4ccccd, v19
	v_max_f32_e32 v16, v16, v46
	v_max_f32_e32 v17, v17, v47
	v_max_f32_e32 v18, v18, v48
	v_max_f32_e32 v19, v19, v49
	v_cmp_lt_i32_e64 s[28:29], 0, v74
	v_cmp_lt_i32_e64 s[30:31], 1, v74
	v_cmp_lt_i32_e64 s[32:33], 2, v74
	v_cmp_lt_i32_e64 s[34:35], 3, v74
	v_cndmask_b32_e64 v16, v51, v16, s[28:29]
	v_cndmask_b32_e64 v17, v51, v17, s[30:31]
	v_cndmask_b32_e64 v18, v51, v18, s[32:33]
	v_cndmask_b32_e64 v19, v51, v19, s[34:35]
	v_max3_f32 v46, v16, v17, v18
	v_max_f32_e32 v46, v46, v19
	v_add_u32_e32 v74, -8, v74
	s_nop 0
	v_mov_b32_dpp v47, v46 row_ror:8 row_mask:0xf bank_mask:0xf
	v_max_f32_e32 v46, v46, v47
	v_max_f32_e32 v47, v33, v46
	v_cmp_neq_f32_e32 vcc, 0xff800000, v47
	s_nop 1
	v_cndmask_b32_e32 v46, 0, v47, vcc
	v_sub_f32_e32 v48, v33, v46
	v_sub_f32_e32 v16, v16, v46
	v_sub_f32_e32 v17, v17, v46
	v_sub_f32_e32 v18, v18, v46
	v_sub_f32_e32 v19, v19, v46
	v_exp_f32_e32 v48, v48
	v_exp_f32_e32 v16, v16
	v_exp_f32_e32 v17, v17
	v_exp_f32_e32 v18, v18
	v_exp_f32_e32 v19, v19
	v_mov_b32_e32 v33, v46
	v_mul_f32_e32 v24, v24, v48
	v_mul_f32_e32 v25, v25, v48
	v_mul_f32_e32 v26, v26, v48
	v_mul_f32_e32 v27, v27, v48
	v_mul_f32_e32 v28, v28, v48
	v_mul_f32_e32 v29, v29, v48
	v_mul_f32_e32 v30, v30, v48
	v_mul_f32_e32 v31, v31, v48
	v_mul_f32_e32 v32, v32, v48
	v_fma_mix_f32 v24, v0, v16, v24 op_sel_hi:[1,0,0]
	v_fma_mix_f32 v25, v0, v16, v25 op_sel:[1,0,0] op_sel_hi:[1,0,0]
	v_fma_mix_f32 v26, v1, v16, v26 op_sel_hi:[1,0,0]
	v_fma_mix_f32 v27, v1, v16, v27 op_sel:[1,0,0] op_sel_hi:[1,0,0]
	v_fma_mix_f32 v28, v2, v16, v28 op_sel_hi:[1,0,0]
	v_fma_mix_f32 v29, v2, v16, v29 op_sel:[1,0,0] op_sel_hi:[1,0,0]
	v_fma_mix_f32 v30, v3, v16, v30 op_sel_hi:[1,0,0]
	v_fma_mix_f32 v31, v3, v16, v31 op_sel:[1,0,0] op_sel_hi:[1,0,0]
	v_fma_mix_f32 v24, v4, v17, v24 op_sel_hi:[1,0,0]
	v_fma_mix_f32 v25, v4, v17, v25 op_sel:[1,0,0] op_sel_hi:[1,0,0]
	v_fma_mix_f32 v26, v5, v17, v26 op_sel_hi:[1,0,0]
	v_fma_mix_f32 v27, v5, v17, v27 op_sel:[1,0,0] op_sel_hi:[1,0,0]
	v_fma_mix_f32 v28, v6, v17, v28 op_sel_hi:[1,0,0]
	v_fma_mix_f32 v29, v6, v17, v29 op_sel:[1,0,0] op_sel_hi:[1,0,0]
	v_fma_mix_f32 v30, v7, v17, v30 op_sel_hi:[1,0,0]
	v_fma_mix_f32 v31, v7, v17, v31 op_sel:[1,0,0] op_sel_hi:[1,0,0]
	v_fma_mix_f32 v24, v8, v18, v24 op_sel_hi:[1,0,0]
	v_fma_mix_f32 v25, v8, v18, v25 op_sel:[1,0,0] op_sel_hi:[1,0,0]
	v_fma_mix_f32 v26, v9, v18, v26 op_sel_hi:[1,0,0]
	v_fma_mix_f32 v27, v9, v18, v27 op_sel:[1,0,0] op_sel_hi:[1,0,0]
	v_fma_mix_f32 v28, v10, v18, v28 op_sel_hi:[1,0,0]
	v_fma_mix_f32 v29, v10, v18, v29 op_sel:[1,0,0] op_sel_hi:[1,0,0]
	v_fma_mix_f32 v30, v11, v18, v30 op_sel_hi:[1,0,0]
	v_fma_mix_f32 v31, v11, v18, v31 op_sel:[1,0,0] op_sel_hi:[1,0,0]
	v_fma_mix_f32 v24, v12, v19, v24 op_sel_hi:[1,0,0]
	v_fma_mix_f32 v25, v12, v19, v25 op_sel:[1,0,0] op_sel_hi:[1,0,0]
	v_fma_mix_f32 v26, v13, v19, v26 op_sel_hi:[1,0,0]
	v_fma_mix_f32 v27, v13, v19, v27 op_sel:[1,0,0] op_sel_hi:[1,0,0]
	v_fma_mix_f32 v28, v14, v19, v28 op_sel_hi:[1,0,0]
	v_fma_mix_f32 v29, v14, v19, v29 op_sel:[1,0,0] op_sel_hi:[1,0,0]
	v_fma_mix_f32 v30, v15, v19, v30 op_sel_hi:[1,0,0]
	v_fma_mix_f32 v31, v15, v19, v31 op_sel:[1,0,0] op_sel_hi:[1,0,0]
	v_add_f32_e32 v46, v16, v17
	v_add_f32_e32 v47, v18, v19
	v_add_f32_e32 v46, v46, v47
	v_add_f32_e32 v32, v32, v46
	s_add_i32 s28, s24, 2
	s_cmp_lt_i32 s28, s23
	s_cbranch_scc0 .Lagg2n_ni_a
	ds_read_b128 v[42:45], v75
	s_waitcnt lgkmcnt(0)
	v_add_u32_e32 v42, v42, v56
	v_add_u32_e32 v43, v43, v56
	v_add_u32_e32 v44, v44, v56
	v_add_u32_e32 v45, v45, v56
	global_load_dwordx4 v[0:3], v42, s[8:9]
	global_load_dwordx4 v[4:7], v43, s[8:9]
	global_load_dwordx4 v[8:11], v44, s[8:9]
	global_load_dwordx4 v[12:15], v45, s[8:9]
	v_add_u32_e32 v75, 32, v75
.Lagg2n_ni_a:
	s_add_i32 s24, s24, 1
	s_cmp_lt_i32 s24, s23
	s_cbranch_scc0 .Lagg2n_pass_done
	s_add_i32 s28, s24, 1
	s_cmp_lt_i32 s28, s23
	s_cbranch_scc1 .Lagg2n_w4_b
	s_waitcnt vmcnt(0)
.Lagg2n_w4_b:
	s_waitcnt vmcnt(4)
	v_mov_b32_dpp v16, v34 row_newbcast:5 row_mask:0xf bank_mask:0x3
	v_mov_b32_dpp v16, v34 row_newbcast:13 row_mask:0xf bank_mask:0xc
	v_mov_b32_dpp v17, v38 row_newbcast:5 row_mask:0xf bank_mask:0x3
	v_mov_b32_dpp v17, v38 row_newbcast:13 row_mask:0xf bank_mask:0xc
	v_mov_b32_dpp v18, v20 row_newbcast:5 row_mask:0xf bank_mask:0x3
	v_mov_b32_dpp v18, v20 row_newbcast:13 row_mask:0xf bank_mask:0xc
	v_mov_b32_dpp v19, v76 row_newbcast:5 row_mask:0xf bank_mask:0x3
	v_mov_b32_dpp v19, v76 row_newbcast:13 row_mask:0xf bank_mask:0xc
	s_nop 0
	v_fma_mix_f32 v16, v16, 1.0, v71 op_sel_hi:[1,0,0]
	v_fma_mix_f32 v17, v17, 1.0, v71 op_sel_hi:[1,0,0]
	v_fma_mix_f32 v18, v18, 1.0, v71 op_sel_hi:[1,0,0]
	v_fma_mix_f32 v19, v19, 1.0, v71 op_sel_hi:[1,0,0]
	v_mul_f32_e32 v46, 0x3e4ccccd, v16
	v_mul_f32_e32 v47, 0x3e4ccccd, v17
	v_mul_f32_e32 v48, 0x3e4ccccd, v18
	v_mul_f32_e32 v49, 0x3e4ccccd, v19
	v_max_f32_e32 v16, v16, v46
	v_max_f32_e32 v17, v17, v47
	v_max_f32_e32 v18, v18, v48
	v_max_f32_e32 v19, v19, v49
	v_cmp_lt_i32_e64 s[28:29], 0, v74
	v_cmp_lt_i32_e64 s[30:31], 1, v74
	v_cmp_lt_i32_e64 s[32:33], 2, v74
	v_cmp_lt_i32_e64 s[34:35], 3, v74
	v_cndmask_b32_e64 v16, v51, v16, s[28:29]
	v_cndmask_b32_e64 v17, v51, v17, s[30:31]
	v_cndmask_b32_e64 v18, v51, v18, s[32:33]
	v_cndmask_b32_e64 v19, v51, v19, s[34:35]
	v_max3_f32 v46, v16, v17, v18
	v_max_f32_e32 v46, v46, v19
	v_add_u32_e32 v74, -8, v74
	s_nop 0
	v_mov_b32_dpp v47, v46 row_ror:8 row_mask:0xf bank_mask:0xf
	v_max_f32_e32 v46, v46, v47
	v_max_f32_e32 v47, v33, v46
	v_cmp_neq_f32_e32 vcc, 0xff800000, v47
	s_nop 1
	v_cndmask_b32_e32 v46, 0, v47, vcc
	v_sub_f32_e32 v48, v33, v46
	v_sub_f32_e32 v16, v16, v46
	v_sub_f32_e32 v17, v17, v46
	v_sub_f32_e32 v18, v18, v46
	v_sub_f32_e32 v19, v19, v46
	v_exp_f32_e32 v48, v48
	v_exp_f32_e32 v16, v16
	v_exp_f32_e32 v17, v17
	v_exp_f32_e32 v18, v18
	v_exp_f32_e32 v19, v19
	v_mov_b32_e32 v33, v46
	v_mul_f32_e32 v24, v24, v48
	v_mul_f32_e32 v25, v25, v48
	v_mul_f32_e32 v26, v26, v48
	v_mul_f32_e32 v27, v27, v48
	v_mul_f32_e32 v28, v28, v48
	v_mul_f32_e32 v29, v29, v48
	v_mul_f32_e32 v30, v30, v48
	v_mul_f32_e32 v31, v31, v48
	v_mul_f32_e32 v32, v32, v48
	v_fma_mix_f32 v24, v34, v16, v24 op_sel_hi:[1,0,0]
	v_fma_mix_f32 v25, v34, v16, v25 op_sel:[1,0,0] op_sel_hi:[1,0,0]
	v_fma_mix_f32 v26, v35, v16, v26 op_sel_hi:[1,0,0]
	v_fma_mix_f32 v27, v35, v16, v27 op_sel:[1,0,0] op_sel_hi:[1,0,0]
	v_fma_mix_f32 v28, v36, v16, v28 op_sel_hi:[1,0,0]
	v_fma_mix_f32 v29, v36, v16, v29 op_sel:[1,0,0] op_sel_hi:[1,0,0]
	v_fma_mix_f32 v30, v37, v16, v30 op_sel_hi:[1,0,0]
	v_fma_mix_f32 v31, v37, v16, v31 op_sel:[1,0,0] op_sel_hi:[1,0,0]
	v_fma_mix_f32 v24, v38, v17, v24 op_sel_hi:[1,0,0]
	v_fma_mix_f32 v25, v38, v17, v25 op_sel:[1,0,0] op_sel_hi:[1,0,0]
	v_fma_mix_f32 v26, v39, v17, v26 op_sel_hi:[1,0,0]
	v_fma_mix_f32 v27, v39, v17, v27 op_sel:[1,0,0] op_sel_hi:[1,0,0]
	v_fma_mix_f32 v28, v40, v17, v28 op_sel_hi:[1,0,0]
	v_fma_mix_f32 v29, v40, v17, v29 op_sel:[1,0,0] op_sel_hi:[1,0,0]
	v_fma_mix_f32 v30, v41, v17, v30 op_sel_hi:[1,0,0]
	v_fma_mix_f32 v31, v41, v17, v31 op_sel:[1,0,0] op_sel_hi:[1,0,0]
	v_fma_mix_f32 v24, v20, v18, v24 op_sel_hi:[1,0,0]
	v_fma_mix_f32 v25, v20, v18, v25 op_sel:[1,0,0] op_sel_hi:[1,0,0]
	v_fma_mix_f32 v26, v21, v18, v26 op_sel_hi:[1,0,0]
	v_fma_mix_f32 v27, v21, v18, v27 op_sel:[1,0,0] op_sel_hi:[1,0,0]
	v_fma_mix_f32 v28, v22, v18, v28 op_sel_hi:[1,0,0]
	v_fma_mix_f32 v29, v22, v18, v29 op_sel:[1,0,0] op_sel_hi:[1,0,0]
	v_fma_mix_f32 v30, v23, v18, v30 op_sel_hi:[1,0,0]
	v_fma_mix_f32 v31, v23, v18, v31 op_sel:[1,0,0] op_sel_hi:[1,0,0]
	v_fma_mix_f32 v24, v76, v19, v24 op_sel_hi:[1,0,0]
	v_fma_mix_f32 v25, v76, v19, v25 op_sel:[1,0,0] op_sel_hi:[1,0,0]
	v_fma_mix_f32 v26, v77, v19, v26 op_sel_hi:[1,0,0]
	v_fma_mix_f32 v27, v77, v19, v27 op_sel:[1,0,0] op_sel_hi:[1,0,0]
	v_fma_mix_f32 v28, v78, v19, v28 op_sel_hi:[1,0,0]
	v_fma_mix_f32 v29, v78, v19, v29 op_sel:[1,0,0] op_sel_hi:[1,0,0]
	v_fma_mix_f32 v30, v79, v19, v30 op_sel_hi:[1,0,0]
	v_fma_mix_f32 v31, v79, v19, v31 op_sel:[1,0,0] op_sel_hi:[1,0,0]
	v_add_f32_e32 v46, v16, v17
	v_add_f32_e32 v47, v18, v19
	v_add_f32_e32 v46, v46, v47
	v_add_f32_e32 v32, v32, v46
	s_add_i32 s28, s24, 2
	s_cmp_lt_i32 s28, s23
	s_cbranch_scc0 .Lagg2n_ni_b
	ds_read_b128 v[42:45], v75
	s_waitcnt lgkmcnt(0)
	v_add_u32_e32 v42, v42, v56
	v_add_u32_e32 v43, v43, v56
	v_add_u32_e32 v44, v44, v56
	v_add_u32_e32 v45, v45, v56
	global_load_dwordx4 v[34:37], v42, s[8:9]
	global_load_dwordx4 v[38:41], v43, s[8:9]
	global_load_dwordx4 v[20:23], v44, s[8:9]
	global_load_dwordx4 v[76:79], v45, s[8:9]
	v_add_u32_e32 v75, 32, v75
.Lagg2n_ni_b:
	s_add_i32 s24, s24, 1
	s_cmp_lt_i32 s24, s23
	s_cbranch_scc1 .Lagg2n_loop
.Lagg2n_pass_done:
	s_add_i32 s22, s22, 64
	s_cmp_lt_i32 s22, s21
	s_cbranch_scc0 .Lagg2n_epi
	v_add_u32_e32 v46, -1, v61
	v_add_u32_e32 v47, v60, v52
	v_add_u32_e32 v47, s22, v47
	v_min_i32_e32 v48, v47, v46
	v_max_i32_e32 v48, 0, v48
	v_lshlrev_b32_e32 v48, 1, v48
	global_load_ushort v42, v48, s[6:7]
	v_add_u32_e32 v48, 16, v47
	v_min_i32_e32 v48, v48, v46
	v_max_i32_e32 v48, 0, v48
	v_lshlrev_b32_e32 v48, 1, v48
	global_load_ushort v43, v48, s[6:7]
	v_add_u32_e32 v48, 32, v47
	v_min_i32_e32 v48, v48, v46
	v_max_i32_e32 v48, 0, v48
	v_lshlrev_b32_e32 v48, 1, v48
	global_load_ushort v44, v48, s[6:7]
	v_add_u32_e32 v48, 48, v47
	v_min_i32_e32 v48, v48, v46
	v_max_i32_e32 v48, 0, v48
	v_lshlrev_b32_e32 v48, 1, v48
	global_load_ushort v45, v48, s[6:7]
	s_waitcnt vmcnt(0)
	v_lshlrev_b32_e32 v42, 7, v42
	v_lshlrev_b32_e32 v43, 7, v43
	v_lshlrev_b32_e32 v44, 7, v44
	v_lshlrev_b32_e32 v45, 7, v45
	ds_write2_b32 v57, v42, v43 offset1:16
	ds_write2_b32 v57, v44, v45 offset0:32 offset1:48
	s_branch .Lagg2n_pass
.Lagg2n_epi:
	ds_read_b128 v[8:11], v50
	ds_read_b128 v[12:15], v50 offset:16
	v_add_f32_dpp v24, v24, v24 row_ror:8 row_mask:0xf bank_mask:0xf
	v_add_f32_dpp v25, v25, v25 row_ror:8 row_mask:0xf bank_mask:0xf
	v_add_f32_dpp v26, v26, v26 row_ror:8 row_mask:0xf bank_mask:0xf
	v_add_f32_dpp v27, v27, v27 row_ror:8 row_mask:0xf bank_mask:0xf
	v_add_f32_dpp v28, v28, v28 row_ror:8 row_mask:0xf bank_mask:0xf
	v_add_f32_dpp v29, v29, v29 row_ror:8 row_mask:0xf bank_mask:0xf
	v_add_f32_dpp v30, v30, v30 row_ror:8 row_mask:0xf bank_mask:0xf
	v_add_f32_dpp v31, v31, v31 row_ror:8 row_mask:0xf bank_mask:0xf
	v_add_f32_dpp v32, v32, v32 row_ror:8 row_mask:0xf bank_mask:0xf
	v_mov_b32_e32 v60, v62
	v_mov_b32_e32 v61, v63
	v_mov_b32_e32 v62, v64
	v_mov_b32_e32 v63, v65
	v_rcp_f32_e32 v46, v32
	v_cmp_lt_f32_e32 vcc, 0, v32
	v_mul_u32_u24_e32 v47, 0xa0, v59
	v_lshl_add_u32 v47, v55, 5, v47
	v_cndmask_b32_e32 v46, 0, v46, vcc
	s_waitcnt lgkmcnt(0)
	v_fma_f32 v0, v24, v46, v8
	v_fma_f32 v1, v25, v46, v9
	v_fma_f32 v2, v26, v46, v10
	v_fma_f32 v3, v27, v46, v11
	v_fma_f32 v4, v28, v46, v12
	v_fma_f32 v5, v29, v46, v13
	v_fma_f32 v6, v30, v46, v14
	v_fma_f32 v7, v31, v46, v15
	s_and_saveexec_b64 s[28:29], s[26:27]
	global_store_dwordx4 v47, v[0:3], s[18:19] nt
	global_store_dwordx4 v47, v[4:7], s[18:19] offset:16 nt
	s_mov_b64 exec, s[28:29]
	s_add_i32 s25, s25, s11
	s_cmpk_ge_i32 s25, 0x30d4
	s_cbranch_scc1 .Lagg2n_end
	v_lshl_or_b32 v59, s25, 2, v53
	s_branch .Lagg2n_quad

	.amdhsa_kernel _Z5k_aggILi1ELi40ELi5ELi5ELb1EEvPKiPKtPKDF16_PKfS7_S7_PvS5_S7_S7_PDF16_PfSA_
		.amdhsa_group_segment_fixed_size 8704
		.amdhsa_private_segment_fixed_size 0
		.amdhsa_kernarg_size 360
		.amdhsa_user_sgpr_count 2
		.amdhsa_user_sgpr_dispatch_ptr 0
		.amdhsa_user_sgpr_queue_ptr 0
		.amdhsa_user_sgpr_kernarg_segment_ptr 1
		.amdhsa_user_sgpr_dispatch_id 0
		.amdhsa_user_sgpr_kernarg_preload_length 0
		.amdhsa_user_sgpr_kernarg_preload_offset 0
		.amdhsa_user_sgpr_private_segment_size 0
		.amdhsa_uses_dynamic_stack 0
		.amdhsa_enable_private_segment 0
		.amdhsa_system_sgpr_workgroup_id_x 1
		.amdhsa_system_sgpr_workgroup_id_y 0
		.amdhsa_system_sgpr_workgroup_id_z 0
		.amdhsa_system_sgpr_workgroup_info 0
		.amdhsa_system_vgpr_workitem_id 0
		.amdhsa_next_free_vgpr 80
		.amdhsa_next_free_sgpr 40
		.amdhsa_accum_offset 80
		.amdhsa_reserve_vcc 1
		.amdhsa_float_round_mode_32 0
		.amdhsa_float_round_mode_16_64 0
		.amdhsa_float_denorm_mode_32 3
		.amdhsa_float_denorm_mode_16_64 3
		.amdhsa_dx10_clamp 1
		.amdhsa_ieee_mode 1
		.amdhsa_fp16_overflow 0
		.amdhsa_tg_split 0
		.amdhsa_exception_fp_ieee_invalid_op 0
		.amdhsa_exception_fp_denorm_src 0
		.amdhsa_exception_fp_ieee_div_zero 0
		.amdhsa_exception_fp_ieee_overflow 0
		.amdhsa_exception_fp_ieee_underflow 0
		.amdhsa_exception_fp_ieee_inexact 0
		.amdhsa_exception_int_div_zero 0
	.end_amdhsa_kernel

amdhsa.kernels:
  - .agpr_count:     0
    .args:
      - .actual_access:  read_only
        .address_space:  global
        .offset:         0
        .size:           8
        .value_kind:     global_buffer
      - .actual_access:  read_only
        .address_space:  global
        .offset:         8
        .size:           8
        .value_kind:     global_buffer
      - .actual_access:  write_only
        .address_space:  global
        .offset:         16
        .size:           8
        .value_kind:     global_buffer
      - .actual_access:  write_only
        .address_space:  global
        .offset:         24
        .size:           8
        .value_kind:     global_buffer
    .group_segment_fixed_size: 32320
    .kernarg_segment_align: 8
    .kernarg_segment_size: 32
    .language:       OpenCL C
    .language_version:
      - 2
      - 0
    .max_flat_workgroup_size: 1024
    .name:           _Z6k_finePKjPKtPiPt
    .private_segment_fixed_size: 0
    .sgpr_count:     71
    .sgpr_spill_count: 0
    .symbol:         _Z6k_finePKjPKtPiPt.kd
    .uniform_work_group_size: 1
    .uses_dynamic_stack: false
    .vgpr_count:     54
    .vgpr_spill_count: 0
    .wavefront_size: 64
  - .agpr_count:     0
    .args:
      - .actual_access:  read_only
        .address_space:  global
        .offset:         0
        .size:           8
        .value_kind:     global_buffer
      - .actual_access:  read_only
        .address_space:  global
        .offset:         8
        .size:           8
        .value_kind:     global_buffer
      - .actual_access:  write_only
        .address_space:  global
        .offset:         16
        .size:           8
        .value_kind:     global_buffer
      - .actual_access:  write_only
        .address_space:  global
        .offset:         24
        .size:           8
        .value_kind:     global_buffer
      - .actual_access:  read_only
        .address_space:  global
        .offset:         32
        .size:           8
        .value_kind:     global_buffer
      - .actual_access:  read_only
        .address_space:  global
        .offset:         40
        .size:           8
        .value_kind:     global_buffer
      - .actual_access:  write_only
        .address_space:  global
        .offset:         48
        .size:           8
        .value_kind:     global_buffer
      - .actual_access:  write_only
        .address_space:  global
        .offset:         56
        .size:           8
        .value_kind:     global_buffer
      - .actual_access:  read_only
        .address_space:  global
        .offset:         64
        .size:           8
        .value_kind:     global_buffer
      - .actual_access:  read_only
        .address_space:  global
        .offset:         72
        .size:           8
        .value_kind:     global_buffer
      - .actual_access:  read_only
        .address_space:  global
        .offset:         80
        .size:           8
        .value_kind:     global_buffer
      - .actual_access:  write_only
        .address_space:  global
        .offset:         88
        .size:           8
        .value_kind:     global_buffer
      - .actual_access:  write_only
        .address_space:  global
        .offset:         96
        .size:           8
        .value_kind:     global_buffer
      - .actual_access:  write_only
        .address_space:  global
        .offset:         104
        .size:           8
        .value_kind:     global_buffer
    .group_segment_fixed_size: 53248
    .kernarg_segment_align: 8
    .kernarg_segment_size: 112
    .language:       OpenCL C
    .language_version:
      - 2
      - 0
    .max_flat_workgroup_size: 256
    .name:           _Z8k_stageAPKiS0_PjPtPKfS4_PDF16_S5_S4_S4_S4_S5_PfS6_
    .private_segment_fixed_size: 0
    .sgpr_count:     75
    .sgpr_spill_count: 0
    .symbol:         _Z8k_stageAPKiS0_PjPtPKfS4_PDF16_S5_S4_S4_S4_S5_PfS6_.kd
    .uniform_work_group_size: 1
    .uses_dynamic_stack: false
    .vgpr_count:     158
    .vgpr_spill_count: 0
    .wavefront_size: 64
  - .agpr_count:     4
    .args:
      - .actual_access:  read_only
        .address_space:  global
        .offset:         0
        .size:           8
        .value_kind:     global_buffer
      - .actual_access:  read_only
        .address_space:  global
        .offset:         8
        .size:           8
        .value_kind:     global_buffer
      - .actual_access:  read_only
        .address_space:  global
        .offset:         16
        .size:           8
        .value_kind:     global_buffer
      - .actual_access:  read_only
        .address_space:  global
        .offset:         24
        .size:           8
        .value_kind:     global_buffer
      - .actual_access:  write_only
        .address_space:  global
        .offset:         32
        .size:           8
        .value_kind:     global_buffer
      - .actual_access:  write_only
        .address_space:  global
        .offset:         40
        .size:           8
        .value_kind:     global_buffer
      - .actual_access:  write_only
        .address_space:  global
        .offset:         48
        .size:           8
        .value_kind:     global_buffer
    .group_segment_fixed_size: 19584
    .kernarg_segment_align: 8
    .kernarg_segment_size: 56
    .language:       OpenCL C
    .language_version:
      - 2
      - 0
    .max_flat_workgroup_size: 256
    .name:           _Z7k_gemm2PKDF16_S0_PKfS2_PDF16_PfS4_
    .private_segment_fixed_size: 0
    .sgpr_count:     30
    .sgpr_spill_count: 0
    .symbol:         _Z7k_gemm2PKDF16_S0_PKfS2_PDF16_PfS4_.kd
    .uniform_work_group_size: 1
    .uses_dynamic_stack: false
    .vgpr_count:     84
    .vgpr_spill_count: 0
    .wavefront_size: 64
  - .agpr_count:     12
    .args:
      - .actual_access:  read_only
        .address_space:  global
        .offset:         0
        .size:           8
        .value_kind:     global_buffer
      - .actual_access:  read_only
        .address_space:  global
        .offset:         8
        .size:           8
        .value_kind:     global_buffer
      - .actual_access:  read_only
        .address_space:  global
        .offset:         16
        .size:           8
        .value_kind:     global_buffer
      - .actual_access:  read_only
        .address_space:  global
        .offset:         24
        .size:           8
        .value_kind:     global_buffer
      - .actual_access:  read_only
        .address_space:  global
        .offset:         32
        .size:           8
        .value_kind:     global_buffer
      - .actual_access:  read_only
        .address_space:  global
        .offset:         40
        .size:           8
        .value_kind:     global_buffer
      - .actual_access:  read_only
        .address_space:  global
        .offset:         48
        .size:           8
        .value_kind:     global_buffer
      - .actual_access:  read_only
        .address_space:  global
        .offset:         56
        .size:           8
        .value_kind:     global_buffer
      - .actual_access:  read_only
        .address_space:  global
        .offset:         64
        .size:           8
        .value_kind:     global_buffer
      - .actual_access:  read_only
        .address_space:  global
        .offset:         72
        .size:           8
        .value_kind:     global_buffer
      - .actual_access:  write_only
        .address_space:  global
        .offset:         80
        .size:           8
        .value_kind:     global_buffer
      - .actual_access:  write_only
        .address_space:  global
        .offset:         88
        .size:           8
        .value_kind:     global_buffer
      - .actual_access:  write_only
        .address_space:  global
        .offset:         96
        .size:           8
        .value_kind:     global_buffer
      - .offset:         104
        .size:           4
        .value_kind:     hidden_block_count_x
      - .offset:         108
        .size:           4
        .value_kind:     hidden_block_count_y
      - .offset:         112
        .size:           4
        .value_kind:     hidden_block_count_z
      - .offset:         116
        .size:           2
        .value_kind:     hidden_group_size_x
      - .offset:         118
        .size:           2
        .value_kind:     hidden_group_size_y
      - .offset:         120
        .size:           2
        .value_kind:     hidden_group_size_z
      - .offset:         122
        .size:           2
        .value_kind:     hidden_remainder_x
      - .offset:         124
        .size:           2
        .value_kind:     hidden_remainder_y
      - .offset:         126
        .size:           2
        .value_kind:     hidden_remainder_z
      - .offset:         144
        .size:           8
        .value_kind:     hidden_global_offset_x
      - .offset:         152
        .size:           8
        .value_kind:     hidden_global_offset_y
      - .offset:         160
        .size:           8
        .value_kind:     hidden_global_offset_z
      - .offset:         168
        .size:           2
        .value_kind:     hidden_grid_dims
    .group_segment_fixed_size: 39168
    .kernarg_segment_align: 8
    .kernarg_segment_size: 360
    .language:       OpenCL C
    .language_version:
      - 2
      - 0
    .max_flat_workgroup_size: 256
    .name:           _Z5k_aggILi4ELi128ELi16ELi16ELb0EEvPKiPKtPKDF16_PKfS7_S7_PvS5_S7_S7_PDF16_PfSA_
    .private_segment_fixed_size: 0
    .sgpr_count:     55
    .sgpr_spill_count: 0
    .symbol:         _Z5k_aggILi4ELi128ELi16ELi16ELb0EEvPKiPKtPKDF16_PKfS7_S7_PvS5_S7_S7_PDF16_PfSA_.kd
    .uniform_work_group_size: 1
    .uses_dynamic_stack: false
    .vgpr_count:     124
    .vgpr_spill_count: 0
    .wavefront_size: 64
  - .agpr_count:     0
    .args:
      - .actual_access:  read_only
        .address_space:  global
        .offset:         0
        .size:           8
        .value_kind:     global_buffer
      - .actual_access:  read_only
        .address_space:  global
        .offset:         8
        .size:           8
        .value_kind:     global_buffer
      - .actual_access:  read_only
        .address_space:  global
        .offset:         16
        .size:           8
        .value_kind:     global_buffer
      - .actual_access:  read_only
        .address_space:  global
        .offset:         24
        .size:           8
        .value_kind:     global_buffer
      - .actual_access:  read_only
        .address_space:  global
        .offset:         32
        .size:           8
        .value_kind:     global_buffer
      - .actual_access:  read_only
        .address_space:  global
        .offset:         40
        .size:           8
        .value_kind:     global_buffer
      - .actual_access:  write_only
        .address_space:  global
        .offset:         48
        .size:           8
        .value_kind:     global_buffer
      - .actual_access:  read_only
        .address_space:  global
        .offset:         56
        .size:           8
        .value_kind:     global_buffer
      - .actual_access:  read_only
        .address_space:  global
        .offset:         64
        .size:           8
        .value_kind:     global_buffer
      - .actual_access:  read_only
        .address_space:  global
        .offset:         72
        .size:           8
        .value_kind:     global_buffer
      - .actual_access:  read_only
        .address_space:  global
        .offset:         80
        .size:           8
        .value_kind:     global_buffer
      - .actual_access:  read_only
        .address_space:  global
        .offset:         88
        .size:           8
        .value_kind:     global_buffer
      - .actual_access:  read_only
        .address_space:  global
        .offset:         96
        .size:           8
        .value_kind:     global_buffer
      - .offset:         104
        .size:           4
        .value_kind:     hidden_block_count_x
      - .offset:         108
        .size:           4
        .value_kind:     hidden_block_count_y
      - .offset:         112
        .size:           4
        .value_kind:     hidden_block_count_z
      - .offset:         116
        .size:           2
        .value_kind:     hidden_group_size_x
      - .offset:         118
        .size:           2
        .value_kind:     hidden_group_size_y
      - .offset:         120
        .size:           2
        .value_kind:     hidden_group_size_z
      - .offset:         122
        .size:           2
        .value_kind:     hidden_remainder_x
      - .offset:         124
        .size:           2
        .value_kind:     hidden_remainder_y
      - .offset:         126
        .size:           2
        .value_kind:     hidden_remainder_z
      - .offset:         144
        .size:           8
        .value_kind:     hidden_global_offset_x
      - .offset:         152
        .size:           8
        .value_kind:     hidden_global_offset_y
      - .offset:         160
        .size:           8
        .value_kind:     hidden_global_offset_z
      - .offset:         168
        .size:           2
        .value_kind:     hidden_grid_dims
    .group_segment_fixed_size: 8704
    .kernarg_segment_align: 8
    .kernarg_segment_size: 360
    .language:       OpenCL C
    .language_version:
      - 2
      - 0
    .max_flat_workgroup_size: 256
    .name:           _Z5k_aggILi1ELi40ELi5ELi5ELb1EEvPKiPKtPKDF16_PKfS7_S7_PvS5_S7_S7_PDF16_PfSA_
    .private_segment_fixed_size: 0
    .sgpr_count:     46
    .sgpr_spill_count: 0
    .symbol:         _Z5k_aggILi1ELi40ELi5ELi5ELb1EEvPKiPKtPKDF16_PKfS7_S7_PvS5_S7_S7_PDF16_PfSA_.kd
    .uniform_work_group_size: 1
    .uses_dynamic_stack: false
    .vgpr_count:     80
    .vgpr_spill_count: 0
    .wavefront_size: 64
